# moe_combine: tile-start lookups via v_readfirstlane + v_readlane from a table vector loaded once per phase (were 8 serialized LDS reads per iteration); in-proj row-scale loads issued before the epilog
# speedup vs baseline: 1.0042x; 1.0042x over previous
.LBB0_638:
	s_lshl_b32 s4, s72, 3
	v_readlane_b32 s14, v254, 32
	s_add_i32 s40, s4, s14
	s_cmpk_gt_i32 s40, 0x3fff
	v_readlane_b32 s15, v254, 33
	s_cbranch_scc1 .LBB0_654
	s_waitcnt lgkmcnt(0)
	s_add_u32 s5, s26, 0x1600000
	s_addc_u32 s6, s27, 0
	s_add_u32 s14, s26, 0x1640000
	s_addc_u32 s15, s27, 0
	s_add_u32 s16, s26, 0x1680000
	s_addc_u32 s17, s27, 0
	s_add_i32 s4, s40, s88
	s_min_i32 s38, s4, 0x3fff
	s_ashr_i32 s39, s38, 31
	s_lshl_b64 s[38:39], s[38:39], 4
	s_add_u32 s42, s16, s38
	s_addc_u32 s43, s17, s39
	global_load_dwordx4 v[22:25], v1, s[42:43]
	s_add_u32 s42, s14, s38
	s_addc_u32 s43, s15, s39
	s_add_u32 s38, s5, s38
	s_addc_u32 s39, s6, s39
	s_ashr_i32 s41, s40, 31
	global_load_dwordx4 v[2:5], v1, s[42:43]
	global_load_dwordx4 v[6:9], v1, s[38:39]
	s_lshl_b64 s[38:39], s[40:41], 4
	s_add_u32 s42, s16, s38
	s_addc_u32 s43, s17, s39
	global_load_dwordx4 v[14:17], v1, s[42:43]
	s_add_u32 s42, s14, s38
	s_addc_u32 s43, s15, s39
	s_add_u32 s38, s5, s38
	s_addc_u32 s39, s6, s39
	global_load_dwordx4 v[10:13], v1, s[42:43]
	global_load_dwordx4 v[18:21], v1, s[38:39]
	s_waitcnt vmcnt(0)
	v_lshlrev_b32_e32 v50, 3, v194
	v_ashrrev_i32_e32 v51, 31, v50
	v_lshl_add_u64 v[26:27], v[50:51], 1, s[26:27]
	s_mov_b64 s[38:39], 0x26000000
	v_lshl_add_u64 v[52:53], v[26:27], 0, s[38:39]
	v_lshl_add_u64 v[28:29], s[26:27], 0, v[50:51]
	s_mov_b64 s[38:39], 0x42000000
	s_waitcnt vmcnt(14)
	v_lshl_add_u64 v[54:55], v[28:29], 0, s[38:39]
	s_mov_b64 s[38:39], 0x2a000000
	v_lshl_add_u64 v[56:57], v[26:27], 0, s[38:39]
	v_cmp_eq_u32_e64 s[38:39], 0, v194
	v_lshl_add_u64 v[58:59], v[50:51], 2, s[36:37]
	global_load_dwordx4 v[136:139], v[58:59], off offset:2048
	global_load_dwordx4 v[140:143], v[58:59], off offset:2064
	global_load_dwordx4 v[144:147], v[58:59], off
	global_load_dwordx4 v[148:151], v[58:59], off offset:16
	v_lshlrev_b32_e32 v152, 2, v194
	v_add_u32_e32 v152, 0x20200, v152
	ds_read_b32 v152, v152
	s_waitcnt lgkmcnt(0)
	s_branch .LBB0_641

.LBB0_641:
	s_add_i32 s4, 0, 0x20200
	v_readfirstlane_b32 s100, v6
	s_add_i32 s36, s40, s88
	s_min_i32 s42, s36, 0x3fff
	s_ashr_i32 s43, s42, 31
	v_mov_b64_e32 v[44:45], v[12:13]
	s_waitcnt lgkmcnt(0)
	s_nop 3
	v_readlane_b32 s100, v152, s100
	s_lshl_b32 s100, s100, 8
	v_add_u32_e32 v2, s100, v2
	v_readfirstlane_b32 s100, v7
	s_lshl_b64 s[42:43], s[42:43], 11
	v_mov_b64_e32 v[42:43], v[10:11]
	v_lshl_add_u64 v[10:11], v[52:53], 0, s[42:43]
	s_add_i32 s37, s90, s40
	s_waitcnt lgkmcnt(0)
	s_nop 3
	v_readlane_b32 s100, v152, s100
	s_lshl_b32 s100, s100, 8
	v_add_u32_e32 v6, s100, v3
	v_readfirstlane_b32 s100, v8
	v_ashrrev_i32_e32 v3, 31, v2
	v_lshlrev_b64 v[2:3], 10, v[2:3]
	v_lshl_add_u64 v[2:3], v[54:55], 0, v[2:3]
	v_ashrrev_i32_e32 v7, 31, v6
	s_waitcnt lgkmcnt(0)
	s_nop 3
	v_readlane_b32 s100, v152, s100
	s_lshl_b32 s100, s100, 8
	v_add_u32_e32 v4, s100, v4
	v_readfirstlane_b32 s100, v9
	global_load_dwordx4 v[34:37], v[10:11], off nt
	global_load_dwordx4 v[30:33], v[10:11], off offset:1024 nt
	global_load_dwordx2 v[74:75], v[2:3], off nt
	global_load_dwordx2 v[72:73], v[2:3], off offset:512 nt
	v_lshlrev_b64 v[2:3], 10, v[6:7]
	v_lshl_add_u64 v[2:3], v[54:55], 0, v[2:3]
	s_waitcnt lgkmcnt(0)
	s_nop 3
	v_readlane_b32 s100, v152, s100
	s_lshl_b32 s100, s100, 8
	v_add_u32_e32 v8, s100, v5
	v_ashrrev_i32_e32 v5, 31, v4
	s_min_i32 s42, s37, 0x3fff
	global_load_dwordx2 v[70:71], v[2:3], off nt
	global_load_dwordx2 v[68:69], v[2:3], off offset:512 nt
	v_lshlrev_b64 v[2:3], 10, v[4:5]
	s_ashr_i32 s43, s42, 31
	v_lshl_add_u64 v[2:3], v[54:55], 0, v[2:3]
	v_ashrrev_i32_e32 v9, 31, v8
	s_lshl_b64 s[42:43], s[42:43], 4
	global_load_dwordx2 v[66:67], v[2:3], off nt
	global_load_dwordx2 v[64:65], v[2:3], off offset:512 nt
	v_lshlrev_b64 v[2:3], 10, v[8:9]
	s_add_u32 s44, s5, s42
	s_waitcnt vmcnt(8)
	v_mov_b64_e32 v[48:49], v[20:21]
	v_lshl_add_u64 v[2:3], v[54:55], 0, v[2:3]
	s_addc_u32 s45, s6, s43
	v_mov_b64_e32 v[46:47], v[18:19]
	global_load_dwordx2 v[62:63], v[2:3], off nt
	global_load_dwordx2 v[60:61], v[2:3], off offset:512 nt
	global_load_dwordx4 v[18:21], v1, s[44:45]
	s_add_u32 s44, s14, s42
	s_addc_u32 s45, s15, s43
	v_readfirstlane_b32 s100, v49
	s_add_u32 s42, s16, s42
	v_mov_b64_e32 v[40:41], v[16:17]
	s_addc_u32 s43, s17, s43
	s_add_i32 s37, s46, s40
	v_mov_b64_e32 v[38:39], v[14:15]
	global_load_dwordx4 v[10:13], v1, s[44:45]
	global_load_dwordx4 v[14:17], v1, s[42:43]
	s_min_i32 s42, s37, 0x3fff
	s_ashr_i32 s43, s42, 31
	s_lshl_b64 s[42:43], s[42:43], 4
	s_add_u32 s44, s5, s42
	s_addc_u32 s45, s6, s43
	s_waitcnt lgkmcnt(0)
	s_nop 3
	v_readlane_b32 s100, v152, s100
	s_lshl_b32 s100, s100, 8
	global_load_dwordx4 v[6:9], v1, s[44:45]
	s_add_u32 s44, s14, s42
	v_add_u32_e32 v76, s100, v45
	s_addc_u32 s45, s15, s43
	v_ashrrev_i32_e32 v77, 31, v76
	s_add_u32 s42, s16, s42
	v_lshlrev_b64 v[76:77], 10, v[76:77]
	v_readfirstlane_b32 s100, v48
	s_addc_u32 s43, s17, s43
	v_lshl_add_u64 v[78:79], v[54:55], 0, v[76:77]
	global_load_dwordx4 v[2:5], v1, s[44:45]
	global_load_dwordx4 v[26:29], v1, s[42:43]
	global_load_dwordx2 v[76:77], v[78:79], off offset:512 nt
	s_nop 0
	global_load_dwordx2 v[78:79], v[78:79], off nt
	s_ashr_i32 s41, s40, 31
	s_lshl_b64 s[42:43], s[40:41], 11
	s_mov_b64 s[44:45], -1
	s_waitcnt lgkmcnt(0)
	s_nop 3
	v_readlane_b32 s100, v152, s100
	s_lshl_b32 s100, s100, 8
	v_add_u32_e32 v44, s100, v44
	v_ashrrev_i32_e32 v45, 31, v44
	v_lshlrev_b64 v[44:45], 10, v[44:45]
	v_readfirstlane_b32 s100, v47
	v_lshl_add_u64 v[44:45], v[54:55], 0, v[44:45]
	global_load_dwordx2 v[80:81], v[44:45], off offset:512 nt
	global_load_dwordx2 v[82:83], v[44:45], off nt
	s_waitcnt lgkmcnt(0)
	s_nop 3
	v_readlane_b32 s100, v152, s100
	s_lshl_b32 s100, s100, 8
	v_add_u32_e32 v44, s100, v43
	v_ashrrev_i32_e32 v45, 31, v44
	v_lshlrev_b64 v[44:45], 10, v[44:45]
	v_readfirstlane_b32 s100, v46
	v_lshl_add_u64 v[44:45], v[54:55], 0, v[44:45]
	global_load_dwordx2 v[84:85], v[44:45], off offset:512 nt
	global_load_dwordx2 v[86:87], v[44:45], off nt
	v_lshl_add_u64 v[46:47], v[52:53], 0, s[42:43]
	s_waitcnt lgkmcnt(0)
	s_nop 3
	v_readlane_b32 s100, v152, s100
	s_lshl_b32 s100, s100, 8
	v_add_u32_e32 v42, s100, v42
	v_ashrrev_i32_e32 v43, 31, v42
	v_lshlrev_b64 v[42:43], 10, v[42:43]
	v_lshl_add_u64 v[42:43], v[54:55], 0, v[42:43]
	global_load_dwordx2 v[88:89], v[42:43], off offset:512 nt
	global_load_dwordx2 v[90:91], v[42:43], off nt
	s_nop 0
	global_load_dwordx4 v[42:45], v[46:47], off offset:1024 nt
	s_nop 0
	global_load_dwordx4 v[46:49], v[46:47], off nt
	v_mov_b32_e32 v0, v41
	s_waitcnt vmcnt(8)
	v_cvt_pk_f32_fp8_sdwa v[130:131], v78 src0_sel:WORD_1
	v_cvt_pk_f32_fp8_e32 v[132:133], v79
	v_cvt_pk_f32_fp8_sdwa v[134:135], v79 src0_sel:WORD_1
	s_waitcnt vmcnt(7)
	v_cvt_pk_f32_fp8_e32 v[122:123], v80
	s_waitcnt vmcnt(6)
	v_cvt_pk_f32_fp8_e32 v[116:117], v82
	v_cvt_pk_f32_fp8_sdwa v[124:125], v80 src0_sel:WORD_1
	v_cvt_pk_f32_fp8_e32 v[126:127], v81
	v_cvt_pk_f32_fp8_sdwa v[128:129], v81 src0_sel:WORD_1
	v_cvt_pk_f32_fp8_e32 v[80:81], v78
	v_cvt_pk_f32_fp8_sdwa v[118:119], v82 src0_sel:WORD_1
	v_cvt_pk_f32_fp8_e32 v[120:121], v83
	v_cvt_pk_f32_fp8_sdwa v[82:83], v83 src0_sel:WORD_1
	s_waitcnt vmcnt(5)
	v_cvt_pk_f32_fp8_e32 v[110:111], v84
	s_waitcnt vmcnt(4)
	v_cvt_pk_f32_fp8_e32 v[104:105], v86
	v_cvt_pk_f32_fp8_sdwa v[106:107], v86 src0_sel:WORD_1
	v_cvt_pk_f32_fp8_e32 v[108:109], v87
	v_cvt_pk_f32_fp8_sdwa v[86:87], v87 src0_sel:WORD_1
	v_cvt_pk_f32_fp8_sdwa v[112:113], v84 src0_sel:WORD_1
	v_cvt_pk_f32_fp8_e32 v[114:115], v85
	v_cvt_pk_f32_fp8_sdwa v[84:85], v85 src0_sel:WORD_1
	s_waitcnt vmcnt(3)
	v_cvt_pk_f32_fp8_e32 v[98:99], v88
	s_waitcnt vmcnt(2)
	v_cvt_pk_f32_fp8_e32 v[92:93], v90
	s_waitcnt vmcnt(0)
	v_lshlrev_b32_e32 v78, 16, v46
	v_and_b32_e32 v79, 0xffff0000, v46
	v_cvt_pk_f32_fp8_sdwa v[94:95], v90 src0_sel:WORD_1
	v_cvt_pk_f32_fp8_e32 v[96:97], v91
	v_cvt_pk_f32_fp8_sdwa v[90:91], v91 src0_sel:WORD_1
	v_pk_fma_f32 v[78:79], v[38:39], v[92:93], v[78:79] op_sel_hi:[0,1,1]
	v_pk_fma_f32 v[78:79], v[38:39], v[104:105], v[78:79] op_sel:[1,0,0]
	v_cvt_pk_f32_fp8_sdwa v[100:101], v88 src0_sel:WORD_1
	v_pk_fma_f32 v[78:79], v[40:41], v[116:117], v[78:79] op_sel_hi:[0,1,1]
	v_pk_fma_f32 v[78:79], v[0:1], v[80:81], v[78:79] op_sel_hi:[0,1,1]
	v_lshlrev_b32_e32 v80, 16, v48
	v_and_b32_e32 v81, 0xffff0000, v48
	v_lshlrev_b32_e32 v48, 16, v49
	v_and_b32_e32 v49, 0xffff0000, v49
	v_pk_fma_f32 v[48:49], v[38:39], v[90:91], v[48:49] op_sel_hi:[0,1,1]
	v_pk_fma_f32 v[48:49], v[38:39], v[86:87], v[48:49] op_sel:[1,0,0]
	v_cvt_pk_f32_fp8_sdwa v[86:87], v76 src0_sel:WORD_1
	v_pk_fma_f32 v[48:49], v[40:41], v[82:83], v[48:49] op_sel_hi:[0,1,1]
	v_cvt_pk_f32_fp8_e32 v[82:83], v76
	v_cvt_pk_f32_fp8_e32 v[90:91], v77
	v_cvt_pk_f32_fp8_sdwa v[92:93], v77 src0_sel:WORD_1
	v_lshlrev_b32_e32 v76, 16, v42
	v_and_b32_e32 v77, 0xffff0000, v42
	v_cvt_pk_f32_fp8_e32 v[102:103], v89
	v_cvt_pk_f32_fp8_sdwa v[88:89], v89 src0_sel:WORD_1
	v_pk_fma_f32 v[76:77], v[38:39], v[98:99], v[76:77] op_sel_hi:[0,1,1]
	v_lshlrev_b32_e32 v46, 16, v47
	v_and_b32_e32 v47, 0xffff0000, v47
	v_pk_fma_f32 v[76:77], v[38:39], v[110:111], v[76:77] op_sel:[1,0,0]
	v_pk_fma_f32 v[46:47], v[38:39], v[94:95], v[46:47] op_sel_hi:[0,1,1]
	v_pk_fma_f32 v[80:81], v[38:39], v[96:97], v[80:81] op_sel_hi:[0,1,1]
	v_pk_fma_f32 v[76:77], v[40:41], v[122:123], v[76:77] op_sel_hi:[0,1,1]
	v_lshlrev_b32_e32 v42, 16, v43
	v_and_b32_e32 v43, 0xffff0000, v43
	v_pk_fma_f32 v[46:47], v[38:39], v[106:107], v[46:47] op_sel:[1,0,0]
	v_pk_fma_f32 v[80:81], v[38:39], v[108:109], v[80:81] op_sel:[1,0,0]
	v_pk_fma_f32 v[76:77], v[0:1], v[82:83], v[76:77] op_sel_hi:[0,1,1]
	v_pk_fma_f32 v[42:43], v[38:39], v[100:101], v[42:43] op_sel_hi:[0,1,1]
	v_lshlrev_b32_e32 v82, 16, v44
	v_and_b32_e32 v83, 0xffff0000, v44
	v_lshlrev_b32_e32 v44, 16, v45
	v_and_b32_e32 v45, 0xffff0000, v45
	v_pk_fma_f32 v[46:47], v[40:41], v[118:119], v[46:47] op_sel_hi:[0,1,1]
	v_pk_fma_f32 v[80:81], v[40:41], v[120:121], v[80:81] op_sel_hi:[0,1,1]
	v_pk_fma_f32 v[42:43], v[38:39], v[112:113], v[42:43] op_sel:[1,0,0]
	v_pk_fma_f32 v[82:83], v[38:39], v[102:103], v[82:83] op_sel_hi:[0,1,1]
	v_pk_fma_f32 v[44:45], v[38:39], v[88:89], v[44:45] op_sel_hi:[0,1,1]
	v_pk_fma_f32 v[46:47], v[0:1], v[130:131], v[46:47] op_sel_hi:[0,1,1]
	v_pk_fma_f32 v[80:81], v[0:1], v[132:133], v[80:81] op_sel_hi:[0,1,1]
	v_pk_fma_f32 v[48:49], v[0:1], v[134:135], v[48:49] op_sel_hi:[0,1,1]
	v_pk_fma_f32 v[42:43], v[40:41], v[124:125], v[42:43] op_sel_hi:[0,1,1]
	v_pk_fma_f32 v[82:83], v[38:39], v[114:115], v[82:83] op_sel:[1,0,0]
	v_pk_fma_f32 v[38:39], v[38:39], v[84:85], v[44:45] op_sel:[1,0,0]
	v_pk_fma_f32 v[42:43], v[0:1], v[86:87], v[42:43] op_sel_hi:[0,1,1]
	v_pk_fma_f32 v[82:83], v[40:41], v[126:127], v[82:83] op_sel_hi:[0,1,1]
	v_pk_fma_f32 v[38:39], v[40:41], v[128:129], v[38:39] op_sel_hi:[0,1,1]
	v_pk_mul_f32 v[40:41], v[78:79], v[78:79]
	v_pk_mul_f32 v[44:45], v[46:47], v[46:47]
	v_pk_mul_f32 v[84:85], v[80:81], v[80:81]
	v_pk_mul_f32 v[86:87], v[48:49], v[48:49]
	v_pk_fma_f32 v[82:83], v[0:1], v[90:91], v[82:83] op_sel_hi:[0,1,1]
	v_pk_fma_f32 v[38:39], v[0:1], v[92:93], v[38:39] op_sel_hi:[0,1,1]
	v_add_f32_e32 v0, v86, v87
	v_add_f32_e32 v84, v84, v85
	v_add_f32_e32 v44, v44, v45
	v_add_f32_e32 v40, v40, v41
	v_pk_mul_f32 v[88:89], v[76:77], v[76:77]
	v_pk_mul_f32 v[90:91], v[42:43], v[42:43]
	v_add_f32_e32 v0, v84, v0
	v_add_f32_e32 v40, v40, v44
	v_add_f32_e32 v0, v40, v0
	v_add_f32_e32 v40, v90, v91
	v_add_f32_e32 v41, v88, v89
	v_pk_mul_f32 v[92:93], v[82:83], v[82:83]
	v_pk_mul_f32 v[94:95], v[38:39], v[38:39]
	v_add_f32_e32 v40, v41, v40
	v_add_f32_e32 v0, v0, v40
	v_add_f32_e32 v40, v94, v95
	v_add_f32_e32 v41, v92, v93
	v_add_f32_e32 v40, v41, v40
	v_add_f32_e32 v0, v0, v40
	s_nop 1
	v_add_f32_dpp v0, v0, v0 quad_perm:[1,0,3,2] row_mask:0xf bank_mask:0xf bound_ctrl:1
	s_nop 1
	v_add_f32_dpp v0, v0, v0 quad_perm:[2,3,0,1] row_mask:0xf bank_mask:0xf bound_ctrl:1
	s_nop 1
	v_add_f32_dpp v0, v0, v0 row_half_mirror row_mask:0xf bank_mask:0xf bound_ctrl:1
	s_nop 1
	v_add_f32_dpp v0, v0, v0 row_mirror row_mask:0xf bank_mask:0xf bound_ctrl:1
	v_mov_b32_e32 v40, v0
	s_nop 1
	v_permlane16_swap_b32_e32 v0, v40
	v_add_f32_e32 v0, v0, v40
	v_mov_b32_e32 v40, v0
	s_nop 1
	v_permlane32_swap_b32_e32 v0, v40
	v_add_f32_e32 v0, v0, v40
	v_fmamk_f32 v0, v0, 0x3a800000, v190
	v_cmp_gt_f32_e32 vcc, s96, v0
	v_mul_f32_e32 v40, 0x4b800000, v0
	s_nop 0
	v_cndmask_b32_e32 v0, v0, v40, vcc
	v_rsq_f32_e32 v0, v0
	s_nop 0
	v_mul_f32_e32 v40, 0x45800000, v0
	v_cndmask_b32_e32 v0, v0, v40, vcc
	s_and_b64 vcc, exec, s[30:31]
	s_cbranch_vccz .LBB0_646
	v_lshl_add_u64 v[40:41], v[56:57], 0, s[42:43]
	v_cvt_pk_bf16_f32 v84, v78, v79
	v_cvt_pk_bf16_f32 v85, v46, v47
	v_cvt_pk_bf16_f32 v86, v80, v81
	v_cvt_pk_bf16_f32 v87, v48, v49
	v_cvt_pk_bf16_f32 v88, v76, v77
	v_cvt_pk_bf16_f32 v89, v42, v43
	v_cvt_pk_bf16_f32 v90, v82, v83
	v_cvt_pk_bf16_f32 v91, v38, v39
	global_store_dwordx4 v[40:41], v[84:87], off
	global_store_dwordx4 v[40:41], v[88:91], off offset:1024
	s_and_saveexec_b64 s[42:43], s[38:39]
	s_cbranch_execz .LBB0_644
	s_lshl_b64 s[44:45], s[40:41], 2
	s_add_u32 s44, s26, s44
	s_addc_u32 s45, s27, s45
	global_store_dword v226, v0, s[44:45]

.LBB0_673:
	s_add_u32 s62, s36, 0xfffc0080
	s_addc_u32 s63, s37, -1
	s_add_i32 s86, 0, 0x10000
	s_cmp_eq_u32 s85, 12
	s_cselect_b32 s65, s6, s63
	s_cselect_b32 s64, s27, s62
	v_add_u32_e32 v0, s86, v208
	s_cselect_b32 s63, s55, s84
	s_cselect_b32 s62, s57, s74
	s_add_i32 s87, 0, 0x14000
	ds_read_b128 v[130:133], v0
	ds_read_b128 v[134:137], v0 offset:1024
	ds_read_b128 v[138:141], v0 offset:2048
	ds_read_b128 v[142:145], v0 offset:3072
	v_add_u32_e32 v0, s87, v208
	ds_read_b128 v[146:149], v0
	ds_read_b128 v[150:153], v0 offset:1024
	ds_read_b128 v[154:157], v0 offset:2048
	ds_read_b128 v[158:161], v0 offset:3072
	v_lshl_add_u64 v[202:203], s[36:37], 0, v[172:173]
	s_add_i32 m0, s68, 0xc000
	ds_read_b128 v[184:187], v210
	ds_read_b128 v[198:201], v210 offset:1024
	ds_read_b128 v[212:215], v210 offset:2048
	ds_read_b128 v[216:219], v210 offset:3072
	ds_read_b128 v[220:223], v210 offset:4096
	ds_read_b128 v[234:237], v210 offset:5120
	ds_read_b128 v[238:241], v210 offset:6144
	ds_read_b128 v[242:245], v210 offset:7168
	global_load_lds_dwordx4 v[202:203], off
	v_lshl_add_u64 v[202:203], s[36:37], 0, v[174:175]
	s_add_i32 m0, s68, 0xe000
	s_nop 0
	global_load_lds_dwordx4 v[202:203], off
	s_waitcnt vmcnt(8)
	s_waitcnt lgkmcnt(0)
	s_barrier
	s_setprio 1
	s_waitcnt lgkmcnt(0)
	v_mfma_f32_16x16x32_bf16 v[126:129], v[130:133], v[184:187], v[126:129]
	v_mfma_f32_16x16x32_bf16 v[122:125], v[138:141], v[184:187], v[122:125]
	v_mfma_f32_16x16x32_bf16 v[118:121], v[130:133], v[212:215], v[118:121]
	v_mfma_f32_16x16x32_bf16 v[114:117], v[138:141], v[212:215], v[114:117]
	v_mfma_f32_16x16x32_bf16 v[94:97], v[130:133], v[220:223], v[94:97]
	v_mfma_f32_16x16x32_bf16 v[90:93], v[138:141], v[220:223], v[90:93]
	v_mfma_f32_16x16x32_bf16 v[86:89], v[130:133], v[238:241], v[86:89]
	v_mfma_f32_16x16x32_bf16 v[82:85], v[138:141], v[238:241], v[82:85]
	v_mfma_f32_16x16x32_bf16 v[126:129], v[134:137], v[198:201], v[126:129]
	v_mfma_f32_16x16x32_bf16 v[122:125], v[142:145], v[198:201], v[122:125]
	v_mfma_f32_16x16x32_bf16 v[118:121], v[134:137], v[216:219], v[118:121]
	v_mfma_f32_16x16x32_bf16 v[114:117], v[142:145], v[216:219], v[114:117]
	v_mfma_f32_16x16x32_bf16 v[94:97], v[134:137], v[234:237], v[94:97]
	v_mfma_f32_16x16x32_bf16 v[90:93], v[142:145], v[234:237], v[90:93]
	v_mfma_f32_16x16x32_bf16 v[86:89], v[134:137], v[242:245], v[86:89]
	v_mfma_f32_16x16x32_bf16 v[82:85], v[142:145], v[242:245], v[82:85]
	s_setprio 0
	s_setprio 1
	v_mfma_f32_16x16x32_bf16 v[110:113], v[146:149], v[184:187], v[110:113]
	v_mfma_f32_16x16x32_bf16 v[106:109], v[154:157], v[184:187], v[106:109]
	v_mfma_f32_16x16x32_bf16 v[102:105], v[146:149], v[212:215], v[102:105]
	v_mfma_f32_16x16x32_bf16 v[98:101], v[154:157], v[212:215], v[98:101]
	v_mfma_f32_16x16x32_bf16 v[78:81], v[146:149], v[220:223], v[78:81]
	v_mfma_f32_16x16x32_bf16 v[74:77], v[154:157], v[220:223], v[74:77]
	v_mfma_f32_16x16x32_bf16 v[70:73], v[146:149], v[238:241], v[70:73]
	v_mfma_f32_16x16x32_bf16 v[66:69], v[154:157], v[238:241], v[66:69]
	v_mfma_f32_16x16x32_bf16 v[110:113], v[150:153], v[198:201], v[110:113]
	v_mfma_f32_16x16x32_bf16 v[106:109], v[158:161], v[198:201], v[106:109]
	v_mfma_f32_16x16x32_bf16 v[102:105], v[150:153], v[216:219], v[102:105]
	v_mfma_f32_16x16x32_bf16 v[98:101], v[158:161], v[216:219], v[98:101]
	v_mfma_f32_16x16x32_bf16 v[78:81], v[150:153], v[234:237], v[78:81]
	v_mfma_f32_16x16x32_bf16 v[74:77], v[158:161], v[234:237], v[74:77]
	v_mfma_f32_16x16x32_bf16 v[70:73], v[150:153], v[242:245], v[70:73]
	v_mfma_f32_16x16x32_bf16 v[66:69], v[158:161], v[242:245], v[66:69]
	s_setprio 0
	s_barrier
	s_add_i32 s86, s86, s67
	v_lshl_add_u64 v[202:203], s[62:63], 0, v[166:167]
	s_mov_b32 m0, s86
	ds_read_b128 v[184:187], v210 offset:16384
	ds_read_b128 v[198:201], v210 offset:17408
	ds_read_b128 v[212:215], v210 offset:18432
	ds_read_b128 v[216:219], v210 offset:19456
	ds_read_b128 v[220:223], v210 offset:20480
	ds_read_b128 v[234:237], v210 offset:21504
	ds_read_b128 v[238:241], v210 offset:22528
	ds_read_b128 v[242:245], v210 offset:23552
	global_load_lds_dwordx4 v[202:203], off
	s_add_i32 m0, s86, 0x2000
	s_add_u32 s92, s62, 0x40000
	v_lshl_add_u64 v[246:247], s[62:63], 0, v[170:171]
	s_addc_u32 s93, s63, 0
	s_add_i32 s86, s87, s67
	global_load_lds_dwordx4 v[246:247], off
	v_lshl_add_u64 v[248:249], s[92:93], 0, v[166:167]
	s_mov_b32 m0, s86
	v_lshl_add_u64 v[250:251], s[64:65], 0, v[168:169]
	global_load_lds_dwordx4 v[248:249], off
	v_lshl_add_u64 v[248:249], s[92:93], 0, v[170:171]
	s_add_i32 m0, s86, 0x2000
	s_nop 0
	global_load_lds_dwordx4 v[248:249], off
	v_lshl_add_u64 v[248:249], s[64:65], 0, v[164:165]
	s_mov_b32 m0, s68
	s_nop 0
	global_load_lds_dwordx4 v[248:249], off
	s_mov_b32 m0, s69
	s_nop 0
	global_load_lds_dwordx4 v[250:251], off
	s_waitcnt vmcnt(8)
	s_waitcnt lgkmcnt(0)
	s_barrier
	s_setprio 1
	s_waitcnt lgkmcnt(0)
	v_mfma_f32_16x16x32_bf16 v[62:65], v[130:133], v[184:187], v[62:65]
	v_mfma_f32_16x16x32_bf16 v[58:61], v[138:141], v[184:187], v[58:61]
	v_mfma_f32_16x16x32_bf16 v[54:57], v[130:133], v[212:215], v[54:57]
	v_mfma_f32_16x16x32_bf16 v[50:53], v[138:141], v[212:215], v[50:53]
	v_mfma_f32_16x16x32_bf16 v[30:33], v[130:133], v[220:223], v[30:33]
	v_mfma_f32_16x16x32_bf16 v[26:29], v[138:141], v[220:223], v[26:29]
	v_mfma_f32_16x16x32_bf16 v[22:25], v[130:133], v[238:241], v[22:25]
	v_mfma_f32_16x16x32_bf16 v[18:21], v[138:141], v[238:241], v[18:21]
	v_mfma_f32_16x16x32_bf16 v[62:65], v[134:137], v[198:201], v[62:65]
	v_mfma_f32_16x16x32_bf16 v[58:61], v[142:145], v[198:201], v[58:61]
	v_mfma_f32_16x16x32_bf16 v[54:57], v[134:137], v[216:219], v[54:57]
	v_mfma_f32_16x16x32_bf16 v[50:53], v[142:145], v[216:219], v[50:53]
	v_mfma_f32_16x16x32_bf16 v[30:33], v[134:137], v[234:237], v[30:33]
	v_mfma_f32_16x16x32_bf16 v[26:29], v[142:145], v[234:237], v[26:29]
	v_mfma_f32_16x16x32_bf16 v[22:25], v[134:137], v[242:245], v[22:25]
	v_mfma_f32_16x16x32_bf16 v[18:21], v[142:145], v[242:245], v[18:21]
	s_setprio 0
	s_setprio 1
	v_mfma_f32_16x16x32_bf16 v[46:49], v[146:149], v[184:187], v[46:49]
	v_mfma_f32_16x16x32_bf16 v[42:45], v[154:157], v[184:187], v[42:45]
	v_mfma_f32_16x16x32_bf16 v[38:41], v[146:149], v[212:215], v[38:41]
	v_mfma_f32_16x16x32_bf16 v[34:37], v[154:157], v[212:215], v[34:37]
	v_mfma_f32_16x16x32_bf16 v[14:17], v[146:149], v[220:223], v[14:17]
	v_mfma_f32_16x16x32_bf16 v[10:13], v[154:157], v[220:223], v[10:13]
	v_mfma_f32_16x16x32_bf16 v[6:9], v[146:149], v[238:241], v[6:9]
	v_mfma_f32_16x16x32_bf16 v[2:5], v[154:157], v[238:241], v[2:5]
	v_mfma_f32_16x16x32_bf16 v[46:49], v[150:153], v[198:201], v[46:49]
	v_mfma_f32_16x16x32_bf16 v[42:45], v[158:161], v[198:201], v[42:45]
	v_mfma_f32_16x16x32_bf16 v[38:41], v[150:153], v[216:219], v[38:41]
	v_mfma_f32_16x16x32_bf16 v[34:37], v[158:161], v[216:219], v[34:37]
	v_mfma_f32_16x16x32_bf16 v[14:17], v[150:153], v[234:237], v[14:17]
	v_mfma_f32_16x16x32_bf16 v[10:13], v[158:161], v[234:237], v[10:13]
	v_mfma_f32_16x16x32_bf16 v[6:9], v[150:153], v[242:245], v[6:9]
	v_mfma_f32_16x16x32_bf16 v[2:5], v[158:161], v[242:245], v[2:5]
	s_setprio 0
	s_barrier
	s_add_i32 s86, 0, 0x18000
	v_add_u32_e32 v0, s86, v208
	s_add_i32 s87, 0, 0x1c000
	ds_read_b128 v[130:133], v0
	ds_read_b128 v[134:137], v0 offset:1024
	ds_read_b128 v[138:141], v0 offset:2048
	ds_read_b128 v[142:145], v0 offset:3072
	v_add_u32_e32 v0, s87, v208
	ds_read_b128 v[146:149], v0
	ds_read_b128 v[150:153], v0 offset:1024
	ds_read_b128 v[154:157], v0 offset:2048
	ds_read_b128 v[158:161], v0 offset:3072
	s_add_u32 s64, s64, 0x40000
	s_addc_u32 s65, s65, 0
	s_mov_b32 m0, s70
	v_lshl_add_u64 v[230:231], s[64:65], 0, v[164:165]
	ds_read_b128 v[184:187], v210 offset:32768
	ds_read_b128 v[198:201], v210 offset:33792
	ds_read_b128 v[212:215], v210 offset:34816
	ds_read_b128 v[216:219], v210 offset:35840
	ds_read_b128 v[220:223], v210 offset:36864
	ds_read_b128 v[234:237], v210 offset:37888
	ds_read_b128 v[238:241], v210 offset:38912
	ds_read_b128 v[242:245], v210 offset:39936
	global_load_lds_dwordx4 v[230:231], off
	v_lshl_add_u64 v[230:231], s[64:65], 0, v[168:169]
	s_mov_b32 m0, s71
	s_nop 0
	global_load_lds_dwordx4 v[230:231], off
	s_waitcnt vmcnt(8)
	s_waitcnt lgkmcnt(0)
	s_barrier
	s_setprio 1
	s_waitcnt lgkmcnt(0)
	v_mfma_f32_16x16x32_bf16 v[126:129], v[130:133], v[184:187], v[126:129]
	v_mfma_f32_16x16x32_bf16 v[122:125], v[138:141], v[184:187], v[122:125]
	v_mfma_f32_16x16x32_bf16 v[118:121], v[130:133], v[212:215], v[118:121]
	v_mfma_f32_16x16x32_bf16 v[114:117], v[138:141], v[212:215], v[114:117]
	v_mfma_f32_16x16x32_bf16 v[94:97], v[130:133], v[220:223], v[94:97]
	v_mfma_f32_16x16x32_bf16 v[90:93], v[138:141], v[220:223], v[90:93]
	v_mfma_f32_16x16x32_bf16 v[86:89], v[130:133], v[238:241], v[86:89]
	v_mfma_f32_16x16x32_bf16 v[82:85], v[138:141], v[238:241], v[82:85]
	v_mfma_f32_16x16x32_bf16 v[126:129], v[134:137], v[198:201], v[126:129]
	v_mfma_f32_16x16x32_bf16 v[122:125], v[142:145], v[198:201], v[122:125]
	v_mfma_f32_16x16x32_bf16 v[118:121], v[134:137], v[216:219], v[118:121]
	v_mfma_f32_16x16x32_bf16 v[114:117], v[142:145], v[216:219], v[114:117]
	v_mfma_f32_16x16x32_bf16 v[94:97], v[134:137], v[234:237], v[94:97]
	v_mfma_f32_16x16x32_bf16 v[90:93], v[142:145], v[234:237], v[90:93]
	v_mfma_f32_16x16x32_bf16 v[86:89], v[134:137], v[242:245], v[86:89]
	v_mfma_f32_16x16x32_bf16 v[82:85], v[142:145], v[242:245], v[82:85]
	s_setprio 0
	s_setprio 1
	v_mfma_f32_16x16x32_bf16 v[110:113], v[146:149], v[184:187], v[110:113]
	v_mfma_f32_16x16x32_bf16 v[106:109], v[154:157], v[184:187], v[106:109]
	v_mfma_f32_16x16x32_bf16 v[102:105], v[146:149], v[212:215], v[102:105]
	v_mfma_f32_16x16x32_bf16 v[98:101], v[154:157], v[212:215], v[98:101]
	v_mfma_f32_16x16x32_bf16 v[78:81], v[146:149], v[220:223], v[78:81]
	v_mfma_f32_16x16x32_bf16 v[74:77], v[154:157], v[220:223], v[74:77]
	v_mfma_f32_16x16x32_bf16 v[70:73], v[146:149], v[238:241], v[70:73]
	v_mfma_f32_16x16x32_bf16 v[66:69], v[154:157], v[238:241], v[66:69]
	v_mfma_f32_16x16x32_bf16 v[110:113], v[150:153], v[198:201], v[110:113]
	v_mfma_f32_16x16x32_bf16 v[106:109], v[158:161], v[198:201], v[106:109]
	v_mfma_f32_16x16x32_bf16 v[102:105], v[150:153], v[216:219], v[102:105]
	v_mfma_f32_16x16x32_bf16 v[98:101], v[158:161], v[216:219], v[98:101]
	v_mfma_f32_16x16x32_bf16 v[78:81], v[150:153], v[234:237], v[78:81]
	v_mfma_f32_16x16x32_bf16 v[74:77], v[158:161], v[234:237], v[74:77]
	v_mfma_f32_16x16x32_bf16 v[70:73], v[150:153], v[242:245], v[70:73]
	v_mfma_f32_16x16x32_bf16 v[66:69], v[158:161], v[242:245], v[66:69]
	s_setprio 0
	s_barrier
	s_add_i32 s64, s86, s67
	v_lshl_add_u64 v[202:203], v[202:203], 0, s[22:23]
	s_mov_b32 m0, s64
	ds_read_b128 v[184:187], v210 offset:49152
	ds_read_b128 v[198:201], v210 offset:50176
	ds_read_b128 v[212:215], v210 offset:51200
	ds_read_b128 v[216:219], v210 offset:52224
	ds_read_b128 v[220:223], v210 offset:53248
	ds_read_b128 v[234:237], v210 offset:54272
	ds_read_b128 v[238:241], v210 offset:55296
	ds_read_b128 v[242:245], v210 offset:56320
	global_load_lds_dwordx4 v[202:203], off
	s_add_i32 m0, s64, 0x2000
	s_add_u32 s62, s62, 0x40080
	v_lshl_add_u64 v[202:203], v[246:247], 0, s[22:23]
	s_addc_u32 s63, s63, 0
	s_add_i32 s64, s87, s67
	global_load_lds_dwordx4 v[202:203], off
	v_lshl_add_u64 v[202:203], s[62:63], 0, v[166:167]
	s_mov_b32 m0, s64
	s_nop 0
	global_load_lds_dwordx4 v[202:203], off
	v_lshl_add_u64 v[202:203], s[62:63], 0, v[170:171]
	s_add_i32 m0, s64, 0x2000
	s_nop 0
	global_load_lds_dwordx4 v[202:203], off
	v_lshl_add_u64 v[202:203], v[248:249], 0, s[22:23]
	s_mov_b32 m0, s78
	s_nop 0
	global_load_lds_dwordx4 v[202:203], off
	v_lshl_add_u64 v[202:203], v[250:251], 0, s[22:23]
	s_mov_b32 m0, s79
	s_nop 0
	global_load_lds_dwordx4 v[202:203], off
	s_waitcnt vmcnt(8)
	s_waitcnt lgkmcnt(0)
	s_barrier
	s_setprio 1
	s_waitcnt lgkmcnt(0)
	v_mfma_f32_16x16x32_bf16 v[62:65], v[130:133], v[184:187], v[62:65]
	v_mfma_f32_16x16x32_bf16 v[58:61], v[138:141], v[184:187], v[58:61]
	v_mfma_f32_16x16x32_bf16 v[54:57], v[130:133], v[212:215], v[54:57]
	v_mfma_f32_16x16x32_bf16 v[50:53], v[138:141], v[212:215], v[50:53]
	v_mfma_f32_16x16x32_bf16 v[30:33], v[130:133], v[220:223], v[30:33]
	v_mfma_f32_16x16x32_bf16 v[26:29], v[138:141], v[220:223], v[26:29]
	v_mfma_f32_16x16x32_bf16 v[22:25], v[130:133], v[238:241], v[22:25]
	v_mfma_f32_16x16x32_bf16 v[18:21], v[138:141], v[238:241], v[18:21]
	v_mfma_f32_16x16x32_bf16 v[62:65], v[134:137], v[198:201], v[62:65]
	v_mfma_f32_16x16x32_bf16 v[58:61], v[142:145], v[198:201], v[58:61]
	v_mfma_f32_16x16x32_bf16 v[54:57], v[134:137], v[216:219], v[54:57]
	v_mfma_f32_16x16x32_bf16 v[50:53], v[142:145], v[216:219], v[50:53]
	v_mfma_f32_16x16x32_bf16 v[30:33], v[134:137], v[234:237], v[30:33]
	v_mfma_f32_16x16x32_bf16 v[26:29], v[142:145], v[234:237], v[26:29]
	v_mfma_f32_16x16x32_bf16 v[22:25], v[134:137], v[242:245], v[22:25]
	v_mfma_f32_16x16x32_bf16 v[18:21], v[142:145], v[242:245], v[18:21]
	s_setprio 0
	s_setprio 1
	v_mfma_f32_16x16x32_bf16 v[46:49], v[146:149], v[184:187], v[46:49]
	v_mfma_f32_16x16x32_bf16 v[42:45], v[154:157], v[184:187], v[42:45]
	v_mfma_f32_16x16x32_bf16 v[38:41], v[146:149], v[212:215], v[38:41]
	v_mfma_f32_16x16x32_bf16 v[34:37], v[154:157], v[212:215], v[34:37]
	v_mfma_f32_16x16x32_bf16 v[14:17], v[146:149], v[220:223], v[14:17]
	v_mfma_f32_16x16x32_bf16 v[10:13], v[154:157], v[220:223], v[10:13]
	v_mfma_f32_16x16x32_bf16 v[6:9], v[146:149], v[238:241], v[6:9]
	v_mfma_f32_16x16x32_bf16 v[2:5], v[154:157], v[238:241], v[2:5]
	v_mfma_f32_16x16x32_bf16 v[46:49], v[150:153], v[198:201], v[46:49]
	v_mfma_f32_16x16x32_bf16 v[42:45], v[158:161], v[198:201], v[42:45]
	v_mfma_f32_16x16x32_bf16 v[38:41], v[150:153], v[216:219], v[38:41]
	v_mfma_f32_16x16x32_bf16 v[34:37], v[158:161], v[216:219], v[34:37]
	v_mfma_f32_16x16x32_bf16 v[14:17], v[150:153], v[234:237], v[14:17]
	v_mfma_f32_16x16x32_bf16 v[10:13], v[158:161], v[234:237], v[10:13]
	v_mfma_f32_16x16x32_bf16 v[6:9], v[150:153], v[242:245], v[6:9]
	v_mfma_f32_16x16x32_bf16 v[2:5], v[158:161], v[242:245], v[2:5]
	s_setprio 0
	s_barrier
	s_add_i32 s85, s85, 2
	s_add_u32 s36, s36, 0x100
	s_addc_u32 s37, s37, 0
	s_add_u32 s74, s74, 0x100
	s_addc_u32 s84, s84, 0
	s_cmp_gt_u32 s85, 13
	s_cbranch_scc0 .LBB0_673
	s_lshl_b32 s57, s26, 8
	s_add_i32 s57, s57, s73
	v_or_b32_e32 v186, s57, v179
	v_ashrrev_i32_e32 v187, 31, v186
	v_lshl_add_u64 v[130:131], v[186:187], 2, s[4:5]
	global_load_dword v206, v[130:131], off
	global_load_dword v204, v[130:131], off offset:64
	global_load_dword v196, v[130:131], off offset:128
	global_load_dword v188, v[130:131], off offset:192
	global_load_dword v182, v[130:131], off offset:512
	global_load_dword v180, v[130:131], off offset:576
	global_load_dword v178, v[130:131], off offset:640
	global_load_dword v176, v[130:131], off offset:704
	s_and_b64 vcc, exec, s[52:53]
	s_cbranch_vccz .LBB0_676
	s_barrier
.LBB0_676:
	s_lshl_b32 s6, s83, 8
	v_add_u32_e32 v184, 0x80, v186
	s_or_b32 s55, s6, s75
	v_ashrrev_i32_e32 v185, 31, v184
	v_or_b32_e32 v198, s55, v207
	s_cmp_gt_i32 s83, 3
	s_mov_b64 s[26:27], -1
	s_cbranch_scc0 .LBB0_683
	s_cmp_gt_u32 s83, 5
	s_cbranch_scc0 .LBB0_679
	s_cmp_eq_u32 s83, 7
	s_cselect_b64 vcc, -1, 0
	v_cndmask_b32_e32 v150, 1.0, v229, vcc
	v_mov_b32_e32 v199, v1
	v_lshlrev_b64 v[130:131], 12, v[186:187]
	v_lshl_add_u64 v[130:131], s[44:45], 0, v[130:131]
	v_lshlrev_b64 v[142:143], 1, v[198:199]
	s_waitcnt vmcnt(0)
	v_mul_f32_e32 v0, v150, v206
	v_lshl_add_u64 v[144:145], v[130:131], 0, v[142:143]
	v_pk_mul_f32 v[132:133], v[128:129], v[0:1] op_sel_hi:[1,0]
	v_pk_mul_f32 v[130:131], v[126:127], v[0:1] op_sel_hi:[1,0]
	v_pk_mul_f32 v[146:147], v[124:125], v[0:1] op_sel_hi:[1,0]
	v_pk_mul_f32 v[148:149], v[122:123], v[0:1] op_sel_hi:[1,0]
	v_cvt_pk_bf16_f32 v130, v130, v131
	v_cvt_pk_bf16_f32 v131, v132, v133
	v_cvt_pk_bf16_f32 v132, v148, v149
	v_cvt_pk_bf16_f32 v133, v146, v147
	v_or_b32_e32 v134, 16, v186
	global_store_dwordx4 v[144:145], v[130:133], off
	v_pk_mul_f32 v[146:147], v[108:109], v[0:1] op_sel_hi:[1,0]
	v_pk_mul_f32 v[148:149], v[106:107], v[0:1] op_sel_hi:[1,0]
	v_pk_mul_f32 v[132:133], v[112:113], v[0:1] op_sel_hi:[1,0]
	v_pk_mul_f32 v[130:131], v[110:111], v[0:1] op_sel_hi:[1,0]
	v_ashrrev_i32_e32 v135, 31, v134
	v_cvt_pk_bf16_f32 v130, v130, v131
	v_cvt_pk_bf16_f32 v131, v132, v133
	v_cvt_pk_bf16_f32 v132, v148, v149
	v_cvt_pk_bf16_f32 v133, v146, v147
	global_store_dwordx4 v[144:145], v[130:133], off offset:256
	v_mul_f32_e32 v0, v150, v204
	v_pk_mul_f32 v[144:145], v[116:117], v[0:1] op_sel_hi:[1,0]
	v_lshlrev_b64 v[130:131], 12, v[134:135]
	v_lshl_add_u64 v[130:131], s[44:45], 0, v[130:131]
	v_lshl_add_u64 v[134:135], v[130:131], 0, v[142:143]
	v_pk_mul_f32 v[132:133], v[120:121], v[0:1] op_sel_hi:[1,0]
	v_pk_mul_f32 v[130:131], v[118:119], v[0:1] op_sel_hi:[1,0]
	v_pk_mul_f32 v[146:147], v[114:115], v[0:1] op_sel_hi:[1,0]
	v_cvt_pk_bf16_f32 v130, v130, v131
	v_cvt_pk_bf16_f32 v131, v132, v133
	v_cvt_pk_bf16_f32 v132, v146, v147
	v_cvt_pk_bf16_f32 v133, v144, v145
	v_or_b32_e32 v136, 32, v186
	global_store_dwordx4 v[134:135], v[130:133], off
	v_pk_mul_f32 v[144:145], v[100:101], v[0:1] op_sel_hi:[1,0]
	v_pk_mul_f32 v[146:147], v[98:99], v[0:1] op_sel_hi:[1,0]
	v_pk_mul_f32 v[132:133], v[104:105], v[0:1] op_sel_hi:[1,0]
	v_pk_mul_f32 v[130:131], v[102:103], v[0:1] op_sel_hi:[1,0]
	v_ashrrev_i32_e32 v137, 31, v136
	v_cvt_pk_bf16_f32 v130, v130, v131
	v_cvt_pk_bf16_f32 v131, v132, v133
	v_cvt_pk_bf16_f32 v132, v146, v147
	v_cvt_pk_bf16_f32 v133, v144, v145
	global_store_dwordx4 v[134:135], v[130:133], off offset:256
	v_mul_f32_e32 v0, v150, v196
	v_pk_mul_f32 v[144:145], v[90:91], v[0:1] op_sel_hi:[1,0]
	v_lshlrev_b64 v[130:131], 12, v[136:137]
	v_lshl_add_u64 v[130:131], s[44:45], 0, v[130:131]
	v_lshl_add_u64 v[134:135], v[130:131], 0, v[142:143]
	v_pk_mul_f32 v[132:133], v[96:97], v[0:1] op_sel_hi:[1,0]
	v_pk_mul_f32 v[130:131], v[94:95], v[0:1] op_sel_hi:[1,0]
	v_pk_mul_f32 v[136:137], v[92:93], v[0:1] op_sel_hi:[1,0]
	v_cvt_pk_bf16_f32 v130, v130, v131
	v_cvt_pk_bf16_f32 v131, v132, v133
	v_cvt_pk_bf16_f32 v132, v144, v145
	v_cvt_pk_bf16_f32 v133, v136, v137
	v_or_b32_e32 v138, 48, v186
	global_store_dwordx4 v[134:135], v[130:133], off
	v_pk_mul_f32 v[136:137], v[76:77], v[0:1] op_sel_hi:[1,0]
	v_pk_mul_f32 v[144:145], v[74:75], v[0:1] op_sel_hi:[1,0]
	v_pk_mul_f32 v[132:133], v[80:81], v[0:1] op_sel_hi:[1,0]
	v_pk_mul_f32 v[130:131], v[78:79], v[0:1] op_sel_hi:[1,0]
	v_ashrrev_i32_e32 v139, 31, v138
	v_cvt_pk_bf16_f32 v130, v130, v131
	v_cvt_pk_bf16_f32 v131, v132, v133
	v_cvt_pk_bf16_f32 v132, v144, v145
	v_cvt_pk_bf16_f32 v133, v136, v137
	global_store_dwordx4 v[134:135], v[130:133], off offset:256
	v_mul_f32_e32 v0, v150, v188
	v_pk_mul_f32 v[136:137], v[84:85], v[0:1] op_sel_hi:[1,0]
	v_lshlrev_b64 v[130:131], 12, v[138:139]
	v_lshl_add_u64 v[130:131], s[44:45], 0, v[130:131]
	v_lshl_add_u64 v[134:135], v[130:131], 0, v[142:143]
	v_pk_mul_f32 v[132:133], v[88:89], v[0:1] op_sel_hi:[1,0]
	v_pk_mul_f32 v[130:131], v[86:87], v[0:1] op_sel_hi:[1,0]
	v_pk_mul_f32 v[138:139], v[82:83], v[0:1] op_sel_hi:[1,0]
	v_cvt_pk_bf16_f32 v130, v130, v131
	v_cvt_pk_bf16_f32 v131, v132, v133
	v_cvt_pk_bf16_f32 v132, v138, v139
	v_cvt_pk_bf16_f32 v133, v136, v137
	global_store_dwordx4 v[134:135], v[130:133], off
	v_pk_mul_f32 v[136:137], v[68:69], v[0:1] op_sel_hi:[1,0]
	v_pk_mul_f32 v[138:139], v[66:67], v[0:1] op_sel_hi:[1,0]
	v_pk_mul_f32 v[132:133], v[72:73], v[0:1] op_sel_hi:[1,0]
	v_pk_mul_f32 v[130:131], v[70:71], v[0:1] op_sel_hi:[1,0]
	v_mul_f32_e32 v0, v150, v182
	v_cvt_pk_bf16_f32 v130, v130, v131
	v_cvt_pk_bf16_f32 v131, v132, v133
	v_cvt_pk_bf16_f32 v132, v138, v139
	v_cvt_pk_bf16_f32 v133, v136, v137
	global_store_dwordx4 v[134:135], v[130:133], off offset:256
	v_pk_mul_f32 v[136:137], v[60:61], v[0:1] op_sel_hi:[1,0]
	v_pk_mul_f32 v[138:139], v[58:59], v[0:1] op_sel_hi:[1,0]
	v_lshlrev_b64 v[130:131], 12, v[184:185]
	v_lshl_add_u64 v[130:131], s[44:45], 0, v[130:131]
	v_lshl_add_u64 v[134:135], v[130:131], 0, v[142:143]
	v_pk_mul_f32 v[132:133], v[64:65], v[0:1] op_sel_hi:[1,0]
	v_pk_mul_f32 v[130:131], v[62:63], v[0:1] op_sel_hi:[1,0]
	v_lshlrev_b64 v[140:141], 12, v[186:187]
	v_cvt_pk_bf16_f32 v130, v130, v131
	v_cvt_pk_bf16_f32 v131, v132, v133
	v_cvt_pk_bf16_f32 v132, v138, v139
	v_cvt_pk_bf16_f32 v133, v136, v137
	global_store_dwordx4 v[134:135], v[130:133], off
	v_pk_mul_f32 v[136:137], v[44:45], v[0:1] op_sel_hi:[1,0]
	v_pk_mul_f32 v[138:139], v[42:43], v[0:1] op_sel_hi:[1,0]
	v_pk_mul_f32 v[132:133], v[48:49], v[0:1] op_sel_hi:[1,0]
	v_pk_mul_f32 v[130:131], v[46:47], v[0:1] op_sel_hi:[1,0]
	v_mul_f32_e32 v0, v150, v180
	v_cvt_pk_bf16_f32 v130, v130, v131
	v_cvt_pk_bf16_f32 v131, v132, v133
	v_cvt_pk_bf16_f32 v132, v138, v139
	v_cvt_pk_bf16_f32 v133, v136, v137
	global_store_dwordx4 v[134:135], v[130:133], off offset:256
	v_pk_mul_f32 v[138:139], v[52:53], v[0:1] op_sel_hi:[1,0]
	s_mov_b32 s6, 0x90000
	v_lshl_add_u64 v[130:131], s[44:45], 0, v[140:141]
	v_lshl_add_u64 v[134:135], v[130:131], 0, v[142:143]
	v_pk_mul_f32 v[132:133], v[56:57], v[0:1] op_sel_hi:[1,0]
	v_pk_mul_f32 v[130:131], v[54:55], v[0:1] op_sel_hi:[1,0]
	v_pk_mul_f32 v[140:141], v[50:51], v[0:1] op_sel_hi:[1,0]
	v_cvt_pk_bf16_f32 v130, v130, v131
	v_cvt_pk_bf16_f32 v131, v132, v133
	v_cvt_pk_bf16_f32 v133, v138, v139
	v_add_co_u32_e32 v138, vcc, s6, v134
	v_cvt_pk_bf16_f32 v132, v140, v141
	s_nop 0
	v_addc_co_u32_e32 v139, vcc, 0, v135, vcc
	s_mov_b64 s[26:27], 0x90000
	global_store_dwordx4 v[138:139], v[130:133], off
	v_pk_mul_f32 v[138:139], v[36:37], v[0:1] op_sel_hi:[1,0]
	v_pk_mul_f32 v[140:141], v[34:35], v[0:1] op_sel_hi:[1,0]
	v_pk_mul_f32 v[132:133], v[40:41], v[0:1] op_sel_hi:[1,0]
	v_pk_mul_f32 v[130:131], v[38:39], v[0:1] op_sel_hi:[1,0]
	v_lshl_add_u64 v[136:137], v[134:135], 0, s[26:27]
	v_cvt_pk_bf16_f32 v130, v130, v131
	v_cvt_pk_bf16_f32 v131, v132, v133
	v_cvt_pk_bf16_f32 v132, v140, v141
	v_cvt_pk_bf16_f32 v133, v138, v139
	v_mul_f32_e32 v0, v150, v178
	global_store_dwordx4 v[136:137], v[130:133], off offset:256
	v_pk_mul_f32 v[138:139], v[28:29], v[0:1] op_sel_hi:[1,0]
	s_mov_b32 s6, 0xa0000
	v_pk_mul_f32 v[132:133], v[32:33], v[0:1] op_sel_hi:[1,0]
	v_pk_mul_f32 v[130:131], v[30:31], v[0:1] op_sel_hi:[1,0]
	v_pk_mul_f32 v[140:141], v[26:27], v[0:1] op_sel_hi:[1,0]
	v_cvt_pk_bf16_f32 v130, v130, v131
	v_cvt_pk_bf16_f32 v131, v132, v133
	v_cvt_pk_bf16_f32 v133, v138, v139
	v_add_co_u32_e32 v138, vcc, s6, v134
	v_cvt_pk_bf16_f32 v132, v140, v141
	s_nop 0
	v_addc_co_u32_e32 v139, vcc, 0, v135, vcc
	s_mov_b64 s[26:27], 0xa0000
	global_store_dwordx4 v[138:139], v[130:133], off
	v_pk_mul_f32 v[138:139], v[12:13], v[0:1] op_sel_hi:[1,0]
	v_pk_mul_f32 v[140:141], v[10:11], v[0:1] op_sel_hi:[1,0]
	v_pk_mul_f32 v[132:133], v[16:17], v[0:1] op_sel_hi:[1,0]
	v_pk_mul_f32 v[130:131], v[14:15], v[0:1] op_sel_hi:[1,0]
	v_lshl_add_u64 v[136:137], v[134:135], 0, s[26:27]
	v_cvt_pk_bf16_f32 v130, v130, v131
	v_cvt_pk_bf16_f32 v131, v132, v133
	v_cvt_pk_bf16_f32 v132, v140, v141
	v_cvt_pk_bf16_f32 v133, v138, v139
	s_mov_b64 s[26:27], 0xb0000
	v_mul_f32_e32 v0, v150, v176
	s_mov_b32 s6, 0xb0000
	global_store_dwordx4 v[136:137], v[130:133], off offset:256
	v_lshl_add_u64 v[136:137], v[134:135], 0, s[26:27]
	v_pk_mul_f32 v[138:139], v[20:21], v[0:1] op_sel_hi:[1,0]
	v_pk_mul_f32 v[132:133], v[24:25], v[0:1] op_sel_hi:[1,0]
	v_pk_mul_f32 v[130:131], v[22:23], v[0:1] op_sel_hi:[1,0]
	v_pk_mul_f32 v[140:141], v[18:19], v[0:1] op_sel_hi:[1,0]
	v_add_co_u32_e32 v134, vcc, s6, v134
	v_cvt_pk_bf16_f32 v130, v130, v131
	v_cvt_pk_bf16_f32 v131, v132, v133
	v_cvt_pk_bf16_f32 v132, v140, v141
	v_cvt_pk_bf16_f32 v133, v138, v139
	v_addc_co_u32_e32 v135, vcc, 0, v135, vcc
	global_store_dwordx4 v[134:135], v[130:133], off
	v_pk_mul_f32 v[134:135], v[4:5], v[0:1] op_sel_hi:[1,0]
	v_pk_mul_f32 v[138:139], v[2:3], v[0:1] op_sel_hi:[1,0]
	v_pk_mul_f32 v[132:133], v[8:9], v[0:1] op_sel_hi:[1,0]
	v_pk_mul_f32 v[130:131], v[6:7], v[0:1] op_sel_hi:[1,0]
	s_mov_b64 s[26:27], 0
	v_cvt_pk_bf16_f32 v130, v130, v131
	v_cvt_pk_bf16_f32 v131, v132, v133
	v_cvt_pk_bf16_f32 v132, v138, v139
	v_cvt_pk_bf16_f32 v133, v134, v135
	global_store_dwordx4 v[136:137], v[130:133], off offset:256
